# w_out GEMM epilogue: X1 stores widened with v_permlane16_swap (2 x dwordx4 per row instead of 4 x dwordx2)
# baseline (speedup 1.0000x reference)
; DI unsigned pk2(float a, float b) { f32x2 f = {a, b}; bf16x2_t h = __builtin_convertvector(f, bf16x2_t); return __builtin_bit_cast(unsigned, h); }
;     __device__ __forceinline__ void operator()(const f32x4 (&acc)[2][2][4][2], const Unit& u, int wr, int wc, int fr, int fq) const {
;         const int row0 = u.a0 * BM + wr * 64 + fr, col0 = u.a1 * BM + wc * 32 + 4 * fq;
;         const int b = (u.a0 * BM) / SEQ; const float* gt = modf + (size_t)b * NMOD + 2 * D;
;         f32x4 gv[2][2];
; #pragma unroll
;         for (int bj = 0; bj < 2; ++bj)
; #pragma unroll
;             for (int n = 0; n < 2; ++n) gv[bj][n] = *(const f32x4*)(gt + col0 + bj * HALF + n * 16) * *(const f32x4*)(wosc + col0 + bj * HALF + n * 16);
; #pragma unroll
;         for (int ai = 0; ai < 2; ++ai)
; #pragma unroll
;             for (int m = 0; m < 4; ++m) { const int row = row0 + ai * HALF + m * 16; const float sr = asc[row]; const size_t off = (size_t)row * D + col0;
; #pragma unroll
;                 for (int bj = 0; bj < 2; ++bj)
; #pragma unroll
;                     for (int n = 0; n < 2; ++n) { const f32x4 xv = *(const f32x4*)(x + off + bj * HALF + n * 16); const f32x4 r = xv + gv[bj][n] * (__builtin_convertvector(__builtin_bit_cast(i32x4_t, acc[ai][bj][m][n]), f32x4) * sr);
;                         u32x2 w; w.x = pk2(r[0], r[1]); w.y = pk2(r[2], r[3]); *(u32x2*)(x1 + off + bj * HALF + n * 16) = w; } }
.LBB0_962:
	v_mbcnt_lo_u32_b32 v252, -1, 0
	v_mbcnt_hi_u32_b32 v252, -1, v252
	v_lshrrev_b32_e32 v252, 4, v252
	v_and_b32_e32 v252, 1, v252
	v_mul_u32_u24_e32 v252, 24, v252
	v_mov_b32_e32 v253, 0
	v_mbcnt_lo_u32_b32 v130, -1, 0
	v_mbcnt_hi_u32_b32 v130, -1, v130
	s_lshl_b32 s2, s67, 8
	s_add_i32 s4, s2, s59
	s_lshl_b32 s2, s68, 8
	v_ashrrev_i32_e32 v128, 2, v130
	s_or_b32 s2, s2, s60
	v_and_b32_e32 v128, -4, v128
	v_add_u32_e32 v132, s2, v128
	s_ashr_i32 s2, s67, 31
	s_lshr_b32 s2, s2, 26
	s_add_i32 s2, s67, s2
	s_ashr_i32 s2, s2, 6
	v_readlane_b32 s68, v254, 2
	s_mul_hi_i32 s3, s2, 0xc000
	s_mul_i32 s2, s2, 0xc000
	v_readlane_b32 s70, v254, 4
	v_readlane_b32 s71, v254, 5
	s_add_u32 s2, s70, s2
	v_ashrrev_i32_e32 v133, 31, v132
	s_addc_u32 s3, s71, s3
	v_lshlrev_b64 v[128:129], 2, v[132:133]
	v_lshl_add_u64 v[166:167], s[2:3], 0, v[128:129]
	v_and_or_b32 v134, v130, 15, s4
	v_lshl_add_u64 v[186:187], s[16:17], 0, v[128:129]
	v_add_co_u32_e32 v128, vcc, s62, v166
	v_ashrrev_i32_e32 v135, 31, v134
	s_nop 0
	v_addc_co_u32_e32 v129, vcc, 0, v167, vcc
	v_lshlrev_b64 v[130:131], 11, v[134:135]
	global_load_dwordx4 v[154:157], v[128:129], off
	global_load_dwordx4 v[158:161], v[186:187], off
	v_lshl_add_u64 v[128:129], v[134:135], 2, s[14:15]
	v_lshl_add_u64 v[130:131], v[130:131], 0, v[132:133]
	global_load_dword v190, v[128:129], off
	v_lshl_add_u64 v[192:193], v[130:131], 2, s[36:37]
	global_load_dwordx4 v[162:165], v[192:193], off
	global_load_dwordx4 v[216:219], v[192:193], off offset:64
	global_load_dwordx4 v[220:223], v[192:193], off offset:512
	global_load_dwordx4 v[224:227], v[192:193], off offset:576
	v_or_b32_e32 v246, 16, v134
	v_ashrrev_i32_e32 v247, 31, v246
	v_lshlrev_b64 v[246:247], 11, v[246:247]
	v_lshl_add_u64 v[246:247], v[246:247], 0, v[132:133]
	v_lshl_add_u64 v[244:245], v[246:247], 2, s[36:37]
	global_load_dwordx4 v[228:231], v[244:245], off
	global_load_dwordx4 v[232:235], v[244:245], off offset:64
	global_load_dwordx4 v[236:239], v[244:245], off offset:512
	global_load_dwordx4 v[240:243], v[244:245], off offset:576
	v_cvt_f32_i32_e32 v127, v127
	v_cvt_f32_i32_e32 v126, v126
	v_cvt_f32_i32_e32 v125, v125
	v_cvt_f32_i32_e32 v124, v124
	v_lshl_add_u64 v[194:195], v[130:131], 1, s[12:13]
	v_lshl_add_u64 v[182:183], v[166:167], 0, s[20:21]
	global_load_dwordx4 v[166:169], v[186:187], off offset:64
	global_load_dwordx4 v[170:173], v[186:187], off offset:512
	global_load_dwordx4 v[174:177], v[182:183], off offset:64
	global_load_dwordx4 v[178:181], v[182:183], off offset:512
	s_nop 0
	global_load_dwordx4 v[182:185], v[182:183], off offset:576
	s_nop 0
	global_load_dwordx4 v[186:189], v[186:187], off offset:576
	v_cvt_f32_i32_e32 v123, v123
	v_cvt_f32_i32_e32 v121, v121
	v_cvt_f32_i32_e32 v120, v120
	v_cvt_f32_i32_e32 v122, v122
	v_cvt_f32_i32_e32 v119, v119
	v_cvt_f32_i32_e32 v117, v117
	v_cvt_f32_i32_e32 v116, v116
	v_cvt_f32_i32_e32 v118, v118
	v_cvt_f32_i32_e32 v115, v115
	v_cvt_f32_i32_e32 v114, v114
	v_cvt_f32_i32_e32 v113, v113
	v_cvt_f32_i32_e32 v112, v112
	v_cvt_f32_i32_e32 v111, v111
	v_cvt_f32_i32_e32 v109, v109
	v_cvt_f32_i32_e32 v108, v108
	v_cvt_f32_i32_e32 v110, v110
	v_cvt_f32_i32_e32 v107, v107
	v_cvt_f32_i32_e32 v105, v105
	v_cvt_f32_i32_e32 v104, v104
	v_cvt_f32_i32_e32 v106, v106
	v_cvt_f32_i32_e32 v103, v103
	v_cvt_f32_i32_e32 v101, v101
	v_cvt_f32_i32_e32 v100, v100
	v_cvt_f32_i32_e32 v102, v102
	v_cvt_f32_i32_e32 v99, v99
	v_cvt_f32_i32_e32 v98, v98
	v_cvt_f32_i32_e32 v97, v97
	v_cvt_f32_i32_e32 v96, v96
	v_cvt_f32_i32_e32 v95, v95
	v_cvt_f32_i32_e32 v93, v93
	v_cvt_f32_i32_e32 v92, v92
	v_cvt_f32_i32_e32 v94, v94
	v_cvt_f32_i32_e32 v91, v91
	v_cvt_f32_i32_e32 v89, v89
	v_cvt_f32_i32_e32 v88, v88
	v_cvt_f32_i32_e32 v90, v90
	v_cvt_f32_i32_e32 v87, v87
	v_cvt_f32_i32_e32 v85, v85
	v_cvt_f32_i32_e32 v84, v84
	v_cvt_f32_i32_e32 v86, v86
	v_cvt_f32_i32_e32 v83, v83
	v_cvt_f32_i32_e32 v82, v82
	v_cvt_f32_i32_e32 v81, v81
	v_cvt_f32_i32_e32 v80, v80
	v_cvt_f32_i32_e32 v79, v79
	v_cvt_f32_i32_e32 v77, v77
	v_cvt_f32_i32_e32 v76, v76
	v_cvt_f32_i32_e32 v78, v78
	v_cvt_f32_i32_e32 v75, v75
	v_cvt_f32_i32_e32 v73, v73
	v_cvt_f32_i32_e32 v72, v72
	v_cvt_f32_i32_e32 v74, v74
	v_cvt_f32_i32_e32 v71, v71
	v_cvt_f32_i32_e32 v69, v69
	v_cvt_f32_i32_e32 v68, v68
	v_cvt_f32_i32_e32 v70, v70
	v_cvt_f32_i32_e32 v67, v67
	v_cvt_f32_i32_e32 v65, v65
	v_cvt_f32_i32_e32 v64, v64
	v_cvt_f32_i32_e32 v66, v66
	v_cvt_f32_i32_e32 v63, v63
	v_cvt_f32_i32_e32 v61, v61
	v_cvt_f32_i32_e32 v60, v60
	v_cvt_f32_i32_e32 v62, v62
	v_cvt_f32_i32_e32 v59, v59
	v_cvt_f32_i32_e32 v57, v57
	v_cvt_f32_i32_e32 v56, v56
	v_cvt_f32_i32_e32 v58, v58
	v_cvt_f32_i32_e32 v55, v55
	v_cvt_f32_i32_e32 v53, v53
	s_waitcnt vmcnt(14)
	v_pk_mul_f32 v[196:197], v[190:191], v[124:125] op_sel_hi:[0,1]
	v_pk_mul_f32 v[198:199], v[190:191], v[126:127] op_sel_hi:[0,1]
	v_pk_mul_f32 v[124:125], v[156:157], v[160:161]
	v_pk_mul_f32 v[126:127], v[154:155], v[158:159]
	s_waitcnt vmcnt(13)
	v_pk_fma_f32 v[154:155], v[124:125], v[198:199], v[164:165]
	v_pk_fma_f32 v[156:157], v[126:127], v[196:197], v[162:163]
	v_pk_mul_f32 v[158:159], v[190:191], v[120:121] op_sel_hi:[0,1]
	v_cvt_pk_bf16_f32 v248, v156, v157
	v_cvt_pk_bf16_f32 v249, v154, v155
	v_pk_mul_f32 v[160:161], v[190:191], v[122:123] op_sel_hi:[0,1]
	s_waitcnt vmcnt(3)
	v_pk_mul_f32 v[120:121], v[176:177], v[168:169]
	v_pk_mul_f32 v[122:123], v[174:175], v[166:167]
	v_pk_mul_f32 v[162:163], v[190:191], v[112:113] op_sel_hi:[0,1]
	v_pk_mul_f32 v[164:165], v[190:191], v[114:115] op_sel_hi:[0,1]
	s_waitcnt vmcnt(0)
; DI unsigned pk2(float a, float b) { f32x2 f = {a, b}; bf16x2_t h = __builtin_convertvector(f, bf16x2_t); return __builtin_bit_cast(unsigned, h); }
;     __device__ __forceinline__ void operator()(const f32x4 (&acc)[2][2][4][2], const Unit& u, int wr, int wc, int fr, int fq) const {
;     ...
;         for (int ai = 0; ai < 2; ++ai)
; #pragma unroll
;             for (int m = 0; m < 4; ++m) { const int row = row0 + ai * HALF + m * 16; const float sr = asc[row]; const size_t off = (size_t)row * D + col0;
; #pragma unroll
;                 for (int bj = 0; bj < 2; ++bj)
; #pragma unroll
;                     for (int n = 0; n < 2; ++n) { const f32x4 xv = *(const f32x4*)(x + off + bj * HALF + n * 16); const f32x4 r = xv + gv[bj][n] * (__builtin_convertvector(__builtin_bit_cast(i32x4_t, acc[ai][bj][m][n]), f32x4) * sr);
;                         u32x2 w; w.x = pk2(r[0], r[1]); w.y = pk2(r[2], r[3]); *(u32x2*)(x1 + off + bj * HALF + n * 16) = w; } }
	v_pk_mul_f32 v[112:113], v[184:185], v[188:189]
	v_pk_mul_f32 v[114:115], v[182:183], v[186:187]
	v_cvt_f32_i32_e32 v52, v52
	v_cvt_f32_i32_e32 v54, v54
	v_cvt_f32_i32_e32 v51, v51
	v_cvt_f32_i32_e32 v49, v49
	v_cvt_f32_i32_e32 v48, v48
	v_cvt_f32_i32_e32 v50, v50
	v_cvt_f32_i32_e32 v47, v47
	v_cvt_f32_i32_e32 v45, v45
	v_cvt_f32_i32_e32 v44, v44
	v_cvt_f32_i32_e32 v46, v46
	v_cvt_f32_i32_e32 v43, v43
	v_cvt_f32_i32_e32 v41, v41
	v_cvt_f32_i32_e32 v40, v40
	v_cvt_f32_i32_e32 v42, v42
	v_cvt_f32_i32_e32 v39, v39
	v_cvt_f32_i32_e32 v37, v37
	v_cvt_f32_i32_e32 v36, v36
	v_cvt_f32_i32_e32 v38, v38
	v_cvt_f32_i32_e32 v35, v35
	v_cvt_f32_i32_e32 v33, v33
	v_cvt_f32_i32_e32 v32, v32
	v_cvt_f32_i32_e32 v34, v34
	v_cvt_f32_i32_e32 v31, v31
	v_cvt_f32_i32_e32 v29, v29
	v_cvt_f32_i32_e32 v28, v28
	v_cvt_f32_i32_e32 v30, v30
	v_cvt_f32_i32_e32 v27, v27
	v_cvt_f32_i32_e32 v25, v25
	v_cvt_f32_i32_e32 v24, v24
	v_cvt_f32_i32_e32 v26, v26
	v_cvt_f32_i32_e32 v23, v23
	v_cvt_f32_i32_e32 v21, v21
	v_cvt_f32_i32_e32 v20, v20
	v_cvt_f32_i32_e32 v22, v22
	v_cvt_f32_i32_e32 v19, v19
	v_cvt_f32_i32_e32 v17, v17
	v_cvt_f32_i32_e32 v16, v16
	v_cvt_f32_i32_e32 v18, v18
	v_cvt_f32_i32_e32 v15, v15
	v_cvt_f32_i32_e32 v13, v13
	v_cvt_f32_i32_e32 v12, v12
	v_cvt_f32_i32_e32 v14, v14
	v_cvt_f32_i32_e32 v11, v11
	v_cvt_f32_i32_e32 v9, v9
	v_cvt_f32_i32_e32 v8, v8
	v_cvt_f32_i32_e32 v10, v10
	v_cvt_f32_i32_e32 v7, v7
	v_cvt_f32_i32_e32 v5, v5
	v_cvt_f32_i32_e32 v4, v4
	v_cvt_f32_i32_e32 v6, v6
	v_cvt_f32_i32_e32 v3, v3
	v_cvt_f32_i32_e32 v2, v2
	v_cvt_f32_i32_e32 v1, v1
	v_cvt_f32_i32_e32 v0, v0
	s_andn2_b64 vcc, exec, s[44:45]
	s_mov_b64 s[2:3], -1
	v_readlane_b32 s69, v254, 3
	v_pk_fma_f32 v[156:157], v[120:121], v[160:161], v[218:219]
	v_pk_fma_f32 v[154:155], v[122:123], v[158:159], v[216:217]
	v_pk_mul_f32 v[158:159], v[190:191], v[116:117] op_sel_hi:[0,1]
	v_cvt_pk_bf16_f32 v250, v154, v155
	v_cvt_pk_bf16_f32 v251, v156, v157
	v_lshl_add_u64 v[210:211], v[194:195], 0, v[252:253]
	s_nop 1
	v_permlane16_swap_b32_e32 v248, v250
	v_permlane16_swap_b32_e32 v249, v251
	global_store_dwordx4 v[210:211], v[248:251], off
	v_pk_mul_f32 v[160:161], v[190:191], v[118:119] op_sel_hi:[0,1]
	v_pk_mul_f32 v[116:117], v[180:181], v[172:173]
	v_pk_mul_f32 v[118:119], v[178:179], v[170:171]
	v_pk_fma_f32 v[156:157], v[116:117], v[160:161], v[222:223]
	v_pk_fma_f32 v[154:155], v[118:119], v[158:159], v[220:221]
	v_or_b32_e32 v158, 16, v134
	v_cvt_pk_bf16_f32 v248, v154, v155
	v_cvt_pk_bf16_f32 v249, v156, v157
	v_ashrrev_i32_e32 v159, 31, v158
	v_lshl_add_u64 v[160:161], v[158:159], 2, s[14:15]
	v_lshlrev_b64 v[158:159], 11, v[158:159]
	v_lshl_add_u64 v[158:159], v[158:159], 0, v[132:133]
	v_pk_fma_f32 v[156:157], v[112:113], v[164:165], v[226:227]
	v_pk_fma_f32 v[154:155], v[114:115], v[162:163], v[224:225]
	v_lshl_add_u64 v[162:163], v[158:159], 2, s[36:37]
	v_cvt_pk_bf16_f32 v250, v154, v155
	v_cvt_pk_bf16_f32 v251, v156, v157
	s_nop 1
	v_permlane16_swap_b32_e32 v248, v250
	v_permlane16_swap_b32_e32 v249, v251
	global_store_dwordx4 v[210:211], v[248:251], off offset:256
	global_load_dword v160, v[160:161], off
	v_lshl_add_u64 v[158:159], v[158:159], 1, s[12:13]
	v_or_b32_e32 v246, 32, v134
	v_ashrrev_i32_e32 v247, 31, v246
	v_lshlrev_b64 v[246:247], 11, v[246:247]
	v_lshl_add_u64 v[246:247], v[246:247], 0, v[132:133]
	v_lshl_add_u64 v[244:245], v[246:247], 2, s[36:37]
	global_load_dwordx4 v[212:215], v[244:245], off
	global_load_dwordx4 v[216:219], v[244:245], off offset:64
	global_load_dwordx4 v[220:223], v[244:245], off offset:512
	global_load_dwordx4 v[224:227], v[244:245], off offset:576
	s_waitcnt vmcnt(4)
	v_pk_mul_f32 v[108:109], v[160:161], v[108:109] op_sel_hi:[0,1]
	v_pk_mul_f32 v[110:111], v[160:161], v[110:111] op_sel_hi:[0,1]
	v_pk_fma_f32 v[110:111], v[124:125], v[110:111], v[230:231]
	v_pk_fma_f32 v[108:109], v[126:127], v[108:109], v[228:229]
	v_pk_mul_f32 v[104:105], v[160:161], v[104:105] op_sel_hi:[0,1]
	v_cvt_pk_bf16_f32 v248, v108, v109
	v_cvt_pk_bf16_f32 v249, v110, v111
	v_pk_mul_f32 v[106:107], v[160:161], v[106:107] op_sel_hi:[0,1]
	v_pk_mul_f32 v[100:101], v[160:161], v[100:101] op_sel_hi:[0,1]
	v_pk_mul_f32 v[102:103], v[160:161], v[102:103] op_sel_hi:[0,1]
	v_pk_mul_f32 v[96:97], v[160:161], v[96:97] op_sel_hi:[0,1]
	v_pk_mul_f32 v[98:99], v[160:161], v[98:99] op_sel_hi:[0,1]
	v_pk_fma_f32 v[106:107], v[120:121], v[106:107], v[234:235]
	v_pk_fma_f32 v[104:105], v[122:123], v[104:105], v[232:233]
	s_nop 0
	v_cvt_pk_bf16_f32 v250, v104, v105
	v_cvt_pk_bf16_f32 v251, v106, v107
	v_lshl_add_u64 v[210:211], v[158:159], 0, v[252:253]
	s_nop 1
	v_permlane16_swap_b32_e32 v248, v250
	v_permlane16_swap_b32_e32 v249, v251
	global_store_dwordx4 v[210:211], v[248:251], off
	v_pk_fma_f32 v[102:103], v[116:117], v[102:103], v[238:239]
	v_pk_fma_f32 v[100:101], v[118:119], v[100:101], v[236:237]
	v_or_b32_e32 v104, 32, v134
	v_cvt_pk_bf16_f32 v248, v100, v101
	v_cvt_pk_bf16_f32 v249, v102, v103
	v_ashrrev_i32_e32 v105, 31, v104
	v_lshl_add_u64 v[106:107], v[104:105], 2, s[14:15]
	v_lshlrev_b64 v[104:105], 11, v[104:105]
	v_lshl_add_u64 v[104:105], v[104:105], 0, v[132:133]
	v_pk_fma_f32 v[98:99], v[112:113], v[98:99], v[242:243]
	v_pk_fma_f32 v[96:97], v[114:115], v[96:97], v[240:241]
	v_lshl_add_u64 v[102:103], v[104:105], 2, s[36:37]
	v_cvt_pk_bf16_f32 v250, v96, v97
	v_cvt_pk_bf16_f32 v251, v98, v99
	s_nop 1
	v_permlane16_swap_b32_e32 v248, v250
	v_permlane16_swap_b32_e32 v249, v251
	global_store_dwordx4 v[210:211], v[248:251], off offset:256
	global_load_dword v100, v[106:107], off
	v_lshl_add_u64 v[104:105], v[104:105], 1, s[12:13]
	v_or_b32_e32 v246, 48, v134
	v_ashrrev_i32_e32 v247, 31, v246
	v_lshlrev_b64 v[246:247], 11, v[246:247]
	v_lshl_add_u64 v[246:247], v[246:247], 0, v[132:133]
	v_lshl_add_u64 v[244:245], v[246:247], 2, s[36:37]
	global_load_dwordx4 v[228:231], v[244:245], off
	global_load_dwordx4 v[232:235], v[244:245], off offset:64
	global_load_dwordx4 v[236:239], v[244:245], off offset:512
	global_load_dwordx4 v[240:243], v[244:245], off offset:576
	s_waitcnt vmcnt(4)
; DI unsigned pk2(float a, float b) { f32x2 f = {a, b}; bf16x2_t h = __builtin_convertvector(f, bf16x2_t); return __builtin_bit_cast(unsigned, h); }
;     __device__ __forceinline__ void operator()(const f32x4 (&acc)[2][2][4][2], const Unit& u, int wr, int wc, int fr, int fq) const {
;     ...
;         for (int ai = 0; ai < 2; ++ai)
; #pragma unroll
;             for (int m = 0; m < 4; ++m) { const int row = row0 + ai * HALF + m * 16; const float sr = asc[row]; const size_t off = (size_t)row * D + col0;
; #pragma unroll
;                 for (int bj = 0; bj < 2; ++bj)
; #pragma unroll
;                     for (int n = 0; n < 2; ++n) { const f32x4 xv = *(const f32x4*)(x + off + bj * HALF + n * 16); const f32x4 r = xv + gv[bj][n] * (__builtin_convertvector(__builtin_bit_cast(i32x4_t, acc[ai][bj][m][n]), f32x4) * sr);
;                         u32x2 w; w.x = pk2(r[0], r[1]); w.y = pk2(r[2], r[3]); *(u32x2*)(x1 + off + bj * HALF + n * 16) = w; } }
	v_pk_mul_f32 v[92:93], v[100:101], v[92:93] op_sel_hi:[0,1]
	v_pk_mul_f32 v[94:95], v[100:101], v[94:95] op_sel_hi:[0,1]
	v_pk_fma_f32 v[94:95], v[124:125], v[94:95], v[214:215]
	v_pk_fma_f32 v[92:93], v[126:127], v[92:93], v[212:213]
	v_pk_mul_f32 v[88:89], v[100:101], v[88:89] op_sel_hi:[0,1]
	v_cvt_pk_bf16_f32 v248, v92, v93
	v_cvt_pk_bf16_f32 v249, v94, v95
	v_pk_mul_f32 v[90:91], v[100:101], v[90:91] op_sel_hi:[0,1]
	v_pk_mul_f32 v[84:85], v[100:101], v[84:85] op_sel_hi:[0,1]
	v_pk_mul_f32 v[86:87], v[100:101], v[86:87] op_sel_hi:[0,1]
	v_pk_mul_f32 v[80:81], v[100:101], v[80:81] op_sel_hi:[0,1]
	v_pk_mul_f32 v[82:83], v[100:101], v[82:83] op_sel_hi:[0,1]
	v_pk_fma_f32 v[90:91], v[120:121], v[90:91], v[218:219]
	v_pk_fma_f32 v[88:89], v[122:123], v[88:89], v[216:217]
	s_nop 0
	v_cvt_pk_bf16_f32 v250, v88, v89
	v_cvt_pk_bf16_f32 v251, v90, v91
	v_lshl_add_u64 v[210:211], v[104:105], 0, v[252:253]
	s_nop 1
	v_permlane16_swap_b32_e32 v248, v250
	v_permlane16_swap_b32_e32 v249, v251
	global_store_dwordx4 v[210:211], v[248:251], off
	v_pk_fma_f32 v[86:87], v[116:117], v[86:87], v[222:223]
	v_pk_fma_f32 v[84:85], v[118:119], v[84:85], v[220:221]
	v_or_b32_e32 v88, 48, v134
	v_cvt_pk_bf16_f32 v248, v84, v85
	v_cvt_pk_bf16_f32 v249, v86, v87
	v_ashrrev_i32_e32 v89, 31, v88
	v_lshl_add_u64 v[90:91], v[88:89], 2, s[14:15]
	v_lshlrev_b64 v[88:89], 11, v[88:89]
	v_lshl_add_u64 v[88:89], v[88:89], 0, v[132:133]
	v_pk_fma_f32 v[82:83], v[112:113], v[82:83], v[226:227]
	v_pk_fma_f32 v[80:81], v[114:115], v[80:81], v[224:225]
	v_lshl_add_u64 v[86:87], v[88:89], 2, s[36:37]
	v_cvt_pk_bf16_f32 v250, v80, v81
	v_cvt_pk_bf16_f32 v251, v82, v83
	s_nop 1
	v_permlane16_swap_b32_e32 v248, v250
	v_permlane16_swap_b32_e32 v249, v251
	global_store_dwordx4 v[210:211], v[248:251], off offset:256
	global_load_dword v84, v[90:91], off
	v_lshl_add_u64 v[88:89], v[88:89], 1, s[12:13]
	v_lshl_add_u64 v[246:247], v[130:131], 0, s[22:23]
	v_lshl_add_u64 v[244:245], v[246:247], 2, s[36:37]
	global_load_dwordx4 v[212:215], v[244:245], off
	global_load_dwordx4 v[216:219], v[244:245], off offset:64
	global_load_dwordx4 v[220:223], v[244:245], off offset:512
	global_load_dwordx4 v[224:227], v[244:245], off offset:576
	s_waitcnt vmcnt(4)
	v_pk_mul_f32 v[76:77], v[84:85], v[76:77] op_sel_hi:[0,1]
	v_pk_mul_f32 v[78:79], v[84:85], v[78:79] op_sel_hi:[0,1]
	v_pk_fma_f32 v[78:79], v[124:125], v[78:79], v[230:231]
	v_pk_fma_f32 v[76:77], v[126:127], v[76:77], v[228:229]
	v_pk_mul_f32 v[72:73], v[84:85], v[72:73] op_sel_hi:[0,1]
	v_cvt_pk_bf16_f32 v248, v76, v77
	v_cvt_pk_bf16_f32 v249, v78, v79
	v_pk_mul_f32 v[74:75], v[84:85], v[74:75] op_sel_hi:[0,1]
	v_pk_mul_f32 v[68:69], v[84:85], v[68:69] op_sel_hi:[0,1]
	v_pk_mul_f32 v[70:71], v[84:85], v[70:71] op_sel_hi:[0,1]
	v_pk_mul_f32 v[64:65], v[84:85], v[64:65] op_sel_hi:[0,1]
	v_pk_mul_f32 v[66:67], v[84:85], v[66:67] op_sel_hi:[0,1]
	v_pk_fma_f32 v[74:75], v[120:121], v[74:75], v[234:235]
	v_pk_fma_f32 v[72:73], v[122:123], v[72:73], v[232:233]
	s_nop 0
	v_cvt_pk_bf16_f32 v250, v72, v73
	v_cvt_pk_bf16_f32 v251, v74, v75
	v_lshl_add_u64 v[210:211], v[88:89], 0, v[252:253]
	s_nop 1
	v_permlane16_swap_b32_e32 v248, v250
	v_permlane16_swap_b32_e32 v249, v251
	global_store_dwordx4 v[210:211], v[248:251], off
	v_pk_fma_f32 v[70:71], v[116:117], v[70:71], v[238:239]
	v_pk_fma_f32 v[68:69], v[118:119], v[68:69], v[236:237]
	v_lshl_add_u64 v[72:73], v[130:131], 0, s[22:23]
	v_cvt_pk_bf16_f32 v248, v68, v69
	v_cvt_pk_bf16_f32 v249, v70, v71
	v_pk_fma_f32 v[66:67], v[112:113], v[66:67], v[242:243]
	v_pk_fma_f32 v[64:65], v[114:115], v[64:65], v[240:241]
	v_lshl_add_u64 v[70:71], v[72:73], 2, s[36:37]
	v_cvt_pk_bf16_f32 v250, v64, v65
	v_cvt_pk_bf16_f32 v251, v66, v67
	s_nop 1
	v_permlane16_swap_b32_e32 v248, v250
	v_permlane16_swap_b32_e32 v249, v251
	global_store_dwordx4 v[210:211], v[248:251], off offset:256
	global_load_dword v68, v[128:129], off offset:512
	v_lshl_add_u64 v[72:73], v[72:73], 1, s[12:13]
	v_lshl_add_u64 v[246:247], v[130:131], 0, s[38:39]
	v_lshl_add_u64 v[244:245], v[246:247], 2, s[36:37]
	global_load_dwordx4 v[228:231], v[244:245], off
	global_load_dwordx4 v[232:235], v[244:245], off offset:64
	global_load_dwordx4 v[236:239], v[244:245], off offset:512
	global_load_dwordx4 v[240:243], v[244:245], off offset:576
	s_waitcnt vmcnt(4)
	v_pk_mul_f32 v[60:61], v[68:69], v[60:61] op_sel_hi:[0,1]
	v_pk_mul_f32 v[62:63], v[68:69], v[62:63] op_sel_hi:[0,1]
	v_pk_fma_f32 v[62:63], v[124:125], v[62:63], v[214:215]
	v_pk_fma_f32 v[60:61], v[126:127], v[60:61], v[212:213]
	v_pk_mul_f32 v[56:57], v[68:69], v[56:57] op_sel_hi:[0,1]
	v_cvt_pk_bf16_f32 v248, v60, v61
	v_cvt_pk_bf16_f32 v249, v62, v63
	v_pk_mul_f32 v[58:59], v[68:69], v[58:59] op_sel_hi:[0,1]
	v_pk_mul_f32 v[52:53], v[68:69], v[52:53] op_sel_hi:[0,1]
	v_pk_mul_f32 v[54:55], v[68:69], v[54:55] op_sel_hi:[0,1]
	v_pk_mul_f32 v[48:49], v[68:69], v[48:49] op_sel_hi:[0,1]
	v_pk_mul_f32 v[50:51], v[68:69], v[50:51] op_sel_hi:[0,1]
	v_pk_fma_f32 v[58:59], v[120:121], v[58:59], v[218:219]
	v_pk_fma_f32 v[56:57], v[122:123], v[56:57], v[216:217]
	s_nop 0
	v_cvt_pk_bf16_f32 v250, v56, v57
	v_cvt_pk_bf16_f32 v251, v58, v59
	v_lshl_add_u64 v[210:211], v[72:73], 0, v[252:253]
	s_nop 1
	v_permlane16_swap_b32_e32 v248, v250
	v_permlane16_swap_b32_e32 v249, v251
	global_store_dwordx4 v[210:211], v[248:251], off
	v_pk_fma_f32 v[54:55], v[116:117], v[54:55], v[222:223]
	v_pk_fma_f32 v[52:53], v[118:119], v[52:53], v[220:221]
	v_lshl_add_u64 v[56:57], v[130:131], 0, s[38:39]
	v_cvt_pk_bf16_f32 v248, v52, v53
	v_cvt_pk_bf16_f32 v249, v54, v55
	v_pk_fma_f32 v[50:51], v[112:113], v[50:51], v[226:227]
	v_pk_fma_f32 v[48:49], v[114:115], v[48:49], v[224:225]
	v_lshl_add_u64 v[54:55], v[56:57], 2, s[36:37]
	v_cvt_pk_bf16_f32 v250, v48, v49
	v_cvt_pk_bf16_f32 v251, v50, v51
	s_nop 1
	v_permlane16_swap_b32_e32 v248, v250
	v_permlane16_swap_b32_e32 v249, v251
	global_store_dwordx4 v[210:211], v[248:251], off offset:256
	global_load_dword v52, v[128:129], off offset:576
	v_lshl_add_u64 v[56:57], v[56:57], 1, s[12:13]
	v_lshl_add_u64 v[246:247], v[130:131], 0, s[40:41]
	v_lshl_add_u64 v[244:245], v[246:247], 2, s[36:37]
	global_load_dwordx4 v[212:215], v[244:245], off
	global_load_dwordx4 v[216:219], v[244:245], off offset:64
	global_load_dwordx4 v[220:223], v[244:245], off offset:512
	global_load_dwordx4 v[224:227], v[244:245], off offset:576
	s_waitcnt vmcnt(4)
; DI unsigned pk2(float a, float b) { f32x2 f = {a, b}; bf16x2_t h = __builtin_convertvector(f, bf16x2_t); return __builtin_bit_cast(unsigned, h); }
;     __device__ __forceinline__ void operator()(const f32x4 (&acc)[2][2][4][2], const Unit& u, int wr, int wc, int fr, int fq) const {
;     ...
;         for (int ai = 0; ai < 2; ++ai)
; #pragma unroll
;             for (int m = 0; m < 4; ++m) { const int row = row0 + ai * HALF + m * 16; const float sr = asc[row]; const size_t off = (size_t)row * D + col0;
; #pragma unroll
;                 for (int bj = 0; bj < 2; ++bj)
; #pragma unroll
;                     for (int n = 0; n < 2; ++n) { const f32x4 xv = *(const f32x4*)(x + off + bj * HALF + n * 16); const f32x4 r = xv + gv[bj][n] * (__builtin_convertvector(__builtin_bit_cast(i32x4_t, acc[ai][bj][m][n]), f32x4) * sr);
;                         u32x2 w; w.x = pk2(r[0], r[1]); w.y = pk2(r[2], r[3]); *(u32x2*)(x1 + off + bj * HALF + n * 16) = w; } }
	v_pk_mul_f32 v[44:45], v[52:53], v[44:45] op_sel_hi:[0,1]
	v_pk_mul_f32 v[46:47], v[52:53], v[46:47] op_sel_hi:[0,1]
	v_pk_fma_f32 v[46:47], v[124:125], v[46:47], v[230:231]
	v_pk_fma_f32 v[44:45], v[126:127], v[44:45], v[228:229]
	v_pk_mul_f32 v[40:41], v[52:53], v[40:41] op_sel_hi:[0,1]
	v_cvt_pk_bf16_f32 v248, v44, v45
	v_cvt_pk_bf16_f32 v249, v46, v47
	v_pk_mul_f32 v[42:43], v[52:53], v[42:43] op_sel_hi:[0,1]
	v_pk_mul_f32 v[36:37], v[52:53], v[36:37] op_sel_hi:[0,1]
	v_pk_mul_f32 v[38:39], v[52:53], v[38:39] op_sel_hi:[0,1]
	v_pk_mul_f32 v[32:33], v[52:53], v[32:33] op_sel_hi:[0,1]
	v_pk_mul_f32 v[34:35], v[52:53], v[34:35] op_sel_hi:[0,1]
	v_pk_fma_f32 v[42:43], v[120:121], v[42:43], v[234:235]
	v_pk_fma_f32 v[40:41], v[122:123], v[40:41], v[232:233]
	s_nop 0
	v_cvt_pk_bf16_f32 v250, v40, v41
	v_cvt_pk_bf16_f32 v251, v42, v43
	v_lshl_add_u64 v[210:211], v[56:57], 0, v[252:253]
	s_nop 1
	v_permlane16_swap_b32_e32 v248, v250
	v_permlane16_swap_b32_e32 v249, v251
	global_store_dwordx4 v[210:211], v[248:251], off
	v_pk_fma_f32 v[38:39], v[116:117], v[38:39], v[238:239]
	v_pk_fma_f32 v[36:37], v[118:119], v[36:37], v[236:237]
	v_lshl_add_u64 v[40:41], v[130:131], 0, s[40:41]
	v_cvt_pk_bf16_f32 v248, v36, v37
	v_cvt_pk_bf16_f32 v249, v38, v39
	v_pk_fma_f32 v[34:35], v[112:113], v[34:35], v[242:243]
	v_pk_fma_f32 v[32:33], v[114:115], v[32:33], v[240:241]
	v_lshl_add_u64 v[38:39], v[40:41], 2, s[36:37]
	v_cvt_pk_bf16_f32 v250, v32, v33
	v_cvt_pk_bf16_f32 v251, v34, v35
	s_nop 1
	v_permlane16_swap_b32_e32 v248, v250
	v_permlane16_swap_b32_e32 v249, v251
	global_store_dwordx4 v[210:211], v[248:251], off offset:256
	global_load_dword v36, v[128:129], off offset:640
	v_lshl_add_u64 v[40:41], v[40:41], 1, s[12:13]
	v_lshl_add_u64 v[246:247], v[130:131], 0, s[42:43]
	v_lshl_add_u64 v[244:245], v[246:247], 2, s[36:37]
	global_load_dwordx4 v[228:231], v[244:245], off
	global_load_dwordx4 v[232:235], v[244:245], off offset:64
	global_load_dwordx4 v[236:239], v[244:245], off offset:512
	global_load_dwordx4 v[240:243], v[244:245], off offset:576
	s_waitcnt vmcnt(4)
	v_pk_mul_f32 v[28:29], v[36:37], v[28:29] op_sel_hi:[0,1]
	v_pk_mul_f32 v[30:31], v[36:37], v[30:31] op_sel_hi:[0,1]
	v_pk_fma_f32 v[30:31], v[124:125], v[30:31], v[214:215]
	v_pk_fma_f32 v[28:29], v[126:127], v[28:29], v[212:213]
	v_pk_mul_f32 v[24:25], v[36:37], v[24:25] op_sel_hi:[0,1]
	v_cvt_pk_bf16_f32 v248, v28, v29
	v_cvt_pk_bf16_f32 v249, v30, v31
	v_pk_mul_f32 v[26:27], v[36:37], v[26:27] op_sel_hi:[0,1]
	v_pk_mul_f32 v[20:21], v[36:37], v[20:21] op_sel_hi:[0,1]
	v_pk_mul_f32 v[22:23], v[36:37], v[22:23] op_sel_hi:[0,1]
	v_pk_mul_f32 v[16:17], v[36:37], v[16:17] op_sel_hi:[0,1]
	v_pk_mul_f32 v[18:19], v[36:37], v[18:19] op_sel_hi:[0,1]
	v_pk_fma_f32 v[26:27], v[120:121], v[26:27], v[218:219]
	v_pk_fma_f32 v[24:25], v[122:123], v[24:25], v[216:217]
	s_nop 0
	v_cvt_pk_bf16_f32 v250, v24, v25
	v_cvt_pk_bf16_f32 v251, v26, v27
	v_lshl_add_u64 v[210:211], v[40:41], 0, v[252:253]
	s_nop 1
	v_permlane16_swap_b32_e32 v248, v250
	v_permlane16_swap_b32_e32 v249, v251
	global_store_dwordx4 v[210:211], v[248:251], off
	v_pk_fma_f32 v[22:23], v[116:117], v[22:23], v[222:223]
	v_pk_fma_f32 v[20:21], v[118:119], v[20:21], v[220:221]
	v_lshl_add_u64 v[24:25], v[130:131], 0, s[42:43]
	v_cvt_pk_bf16_f32 v248, v20, v21
	v_cvt_pk_bf16_f32 v249, v22, v23
	v_pk_fma_f32 v[18:19], v[112:113], v[18:19], v[226:227]
	v_pk_fma_f32 v[16:17], v[114:115], v[16:17], v[224:225]
	v_lshl_add_u64 v[22:23], v[24:25], 2, s[36:37]
	v_cvt_pk_bf16_f32 v250, v16, v17
	v_cvt_pk_bf16_f32 v251, v18, v19
	s_nop 1
	v_permlane16_swap_b32_e32 v248, v250
	v_permlane16_swap_b32_e32 v249, v251
	global_store_dwordx4 v[210:211], v[248:251], off offset:256
	global_load_dword v20, v[128:129], off offset:704
	v_lshl_add_u64 v[24:25], v[24:25], 1, s[12:13]
	s_waitcnt vmcnt(0)
	v_pk_mul_f32 v[12:13], v[20:21], v[12:13] op_sel_hi:[0,1]
	v_pk_mul_f32 v[14:15], v[20:21], v[14:15] op_sel_hi:[0,1]
	v_pk_fma_f32 v[14:15], v[124:125], v[14:15], v[230:231]
	v_pk_fma_f32 v[12:13], v[126:127], v[12:13], v[228:229]
	v_pk_mul_f32 v[8:9], v[20:21], v[8:9] op_sel_hi:[0,1]
	v_cvt_pk_bf16_f32 v248, v12, v13
	v_cvt_pk_bf16_f32 v249, v14, v15
	v_pk_mul_f32 v[10:11], v[20:21], v[10:11] op_sel_hi:[0,1]
	v_pk_mul_f32 v[4:5], v[20:21], v[4:5] op_sel_hi:[0,1]
	v_pk_mul_f32 v[6:7], v[20:21], v[6:7] op_sel_hi:[0,1]
	v_pk_mul_f32 v[0:1], v[20:21], v[0:1] op_sel_hi:[0,1]
	v_pk_mul_f32 v[2:3], v[20:21], v[2:3] op_sel_hi:[0,1]
	v_pk_fma_f32 v[10:11], v[120:121], v[10:11], v[234:235]
	v_pk_fma_f32 v[8:9], v[122:123], v[8:9], v[232:233]
	s_nop 0
	v_cvt_pk_bf16_f32 v250, v8, v9
	v_cvt_pk_bf16_f32 v251, v10, v11
	v_lshl_add_u64 v[210:211], v[24:25], 0, v[252:253]
	s_nop 1
	v_permlane16_swap_b32_e32 v248, v250
	v_permlane16_swap_b32_e32 v249, v251
	global_store_dwordx4 v[210:211], v[248:251], off
	v_pk_fma_f32 v[6:7], v[116:117], v[6:7], v[238:239]
	v_pk_fma_f32 v[4:5], v[118:119], v[4:5], v[236:237]
	s_nop 0
	v_cvt_pk_bf16_f32 v248, v4, v5
	v_cvt_pk_bf16_f32 v249, v6, v7
	v_pk_fma_f32 v[2:3], v[112:113], v[2:3], v[242:243]
	v_pk_fma_f32 v[0:1], v[114:115], v[0:1], v[240:241]
	s_nop 0
	v_cvt_pk_bf16_f32 v250, v0, v1
	v_cvt_pk_bf16_f32 v251, v2, v3
	s_nop 1
	v_permlane16_swap_b32_e32 v248, v250
	v_permlane16_swap_b32_e32 v249, v251
	global_store_dwordx4 v[210:211], v[248:251], off offset:256
	s_cbranch_vccnz .LBB0_951
	s_andn2_b64 vcc, exec, s[10:11]
	s_cbranch_vccnz .LBB0_950
	s_barrier
	s_branch .LBB0_950
